# LN1 row loop: the next row's loads are issued as soon as the current row has been copied out of the prefetch registers (was load-then-wait at the loop top)
# baseline (speedup 1.0000x reference)
; __device__ __forceinline__ void ph_ln1(const In& in, unsigned char* ws, float* r1, int gw, int NGW, int lane) {
;     const float* mod = (const float*)(ws + WS_MOD);
;     const RowV g = row_load(in.ln1_g, lane), bb = row_load(in.ln1_b, lane);
;     for (int row = gw; row < MTOK; row += NGW) { const int b = row >> 13;
;         RowV r = row_load_bf16((const bf16_t*)(r1 + (size_t)row * DM), lane); float mean, rstd; row_norm_stats(r, mean, rstd);
.LBB0_1598:
	s_cmp_lt_i32 s66, 9
	s_cselect_b64 s[0:1], -1, 0
	s_and_b64 s[10:11], s[0:1], s[6:7]
	s_andn2_b64 vcc, exec, s[10:11]
	s_cbranch_vccnz .LBB0_1624
	s_mov_b64 s[6:7], s[76:77]
	s_waitcnt lgkmcnt(0)
	s_load_dwordx4 s[12:15], s[6:7], 0xb8
	s_load_dwordx2 s[16:17], s[6:7], 0x100
	s_cmp_gt_i32 s84, 0xffff
	s_cbranch_scc1 .LBB0_1604
	s_load_dwordx4 s[0:3], s[6:7], 0x98
	s_load_dwordx2 s[4:5], s[6:7], 0xf8
	v_lshlrev_b32_e32 v1, 4, v150
	v_mov_b32_e32 v35, 0
	v_cmp_eq_u32_e64 s[6:7], 0, v150
	s_waitcnt lgkmcnt(0)
	global_load_dwordx4 v[2:5], v1, s[0:1]
	global_load_dwordx4 v[6:9], v1, s[2:3]
	global_load_dwordx4 v[10:13], v1, s[0:1] offset:1024
	global_load_dwordx4 v[14:17], v1, s[2:3] offset:1024
	global_load_dwordx4 v[18:21], v1, s[0:1] offset:2048
	global_load_dwordx4 v[22:25], v1, s[2:3] offset:2048
	global_load_dwordx4 v[26:29], v1, s[0:1] offset:3072
	global_load_dwordx4 v[30:33], v1, s[2:3] offset:3072
	v_mbcnt_lo_u32_b32 v1, -1, 0
	v_mbcnt_hi_u32_b32 v34, -1, v1
	v_and_b32_e32 v1, 64, v34
	v_add_u32_e32 v36, 64, v1
	v_xor_b32_e32 v1, 1, v34
	v_cmp_lt_i32_e32 vcc, v1, v36
	v_xor_b32_e32 v37, 2, v34
	s_add_u32 s0, s16, 0x100000
	v_cndmask_b32_e32 v1, v34, v1, vcc
	v_cmp_lt_i32_e32 vcc, v37, v36
	s_addc_u32 s1, s17, 0
	s_ashr_i32 s85, s84, 31
	v_cndmask_b32_e32 v37, v34, v37, vcc
	v_lshlrev_b32_e32 v62, 2, v37
	v_xor_b32_e32 v37, 4, v34
	v_cmp_lt_i32_e32 vcc, v37, v36
	s_lshl_b64 s[2:3], s[84:85], 3
	s_add_u32 s2, s16, s2
	v_cndmask_b32_e32 v37, v34, v37, vcc
	v_lshlrev_b32_e32 v63, 2, v37
	v_xor_b32_e32 v37, 8, v34
	v_cmp_lt_i32_e32 vcc, v37, v36
	s_addc_u32 s3, s17, s3
	s_add_u32 s18, s2, 0x3c500000
	v_cndmask_b32_e32 v37, v34, v37, vcc
	v_lshlrev_b32_e32 v64, 2, v37
	v_xor_b32_e32 v37, 16, v34
	v_cmp_lt_i32_e32 vcc, v37, v36
	s_addc_u32 s19, s3, 0
	s_ashr_i32 s89, s88, 31
	v_cndmask_b32_e32 v37, v34, v37, vcc
	s_lshl_b64 s[20:21], s[88:89], 3
	s_lshl_b64 s[2:3], s[84:85], 11
	v_lshlrev_b32_e32 v65, 2, v37
	v_xor_b32_e32 v37, 32, v34
	s_add_u32 s22, s16, s2
	v_cmp_lt_i32_e32 vcc, v37, v36
	s_addc_u32 s23, s17, s3
	s_lshl_b64 s[24:25], s[88:89], 11
	s_lshl_b64 s[2:3], s[84:85], 12
	v_cndmask_b32_e32 v34, v34, v37, vcc
	s_add_u32 s26, s4, s2
	v_lshlrev_b32_e32 v1, 2, v1
	v_lshlrev_b32_e32 v66, 2, v34
	v_lshlrev_b32_e32 v36, 3, v150
	v_mov_b32_e32 v37, v35
	s_addc_u32 s27, s5, s3
	s_lshl_b64 s[28:29], s[88:89], 12
	v_mov_b32_e32 v67, 0x3727c5ac
	s_mov_b32 s2, 0xf800000
	v_mov_b32_e32 v68, 0x260
	v_lshlrev_b32_e32 v34, 4, v150
	s_mov_b64 s[30:31], 0x3000
	s_mov_b64 s[40:41], 0x4000
	s_movk_i32 s3, 0x4000
	s_mov_b32 s4, 0x1800000
	s_mov_b32 s5, s84
	v_lshl_add_u64 v[108:109], s[26:27], 0, v[36:37]
	global_load_dwordx2 v[100:101], v[108:109], off offset:1024
	global_load_dwordx2 v[102:103], v[108:109], off offset:1536
	global_load_dwordx2 v[104:105], v[108:109], off
	global_load_dwordx2 v[106:107], v[108:109], off offset:512
	s_waitcnt vmcnt(0)
	s_branch .LBB0_1602

; __device__ __forceinline__ void row_norm_stats(RowV& r, float& mean_o, float& rstd_o) {
;     float s = 0.f;
; #pragma unroll
;     for (int j = 0; j < 4; ++j) s += (r.v[j].x + r.v[j].y) + (r.v[j].z + r.v[j].w);
;     const float mean = wave_sum(s) * (1.f / DM); float s2 = 0.f;
; #pragma unroll
;     for (int j = 0; j < 4; ++j) { r.v[j] = r.v[j] - mean; s2 += (r.v[j].x * r.v[j].x + r.v[j].y * r.v[j].y) + (r.v[j].z * r.v[j].z + r.v[j].w * r.v[j].w); }
;     const float rstd = 1.f / sqrtf(wave_sum(s2) * (1.f / DM) + LN_EPS);
; #pragma unroll
;     for (int j = 0; j < 4; ++j) r.v[j] = r.v[j] * rstd;
;     mean_o = mean; rstd_o = rstd;
; }
; __device__ __forceinline__ void ph_ln1(const In& in, unsigned char* ws, float* r1, int gw, int NGW, int lane) {
;     ...
;     for (int row = gw; row < MTOK; row += NGW) { const int b = row >> 13;
;         RowV r = row_load_bf16((const bf16_t*)(r1 + (size_t)row * DM), lane); float mean, rstd; row_norm_stats(r, mean, rstd);
;         if (lane == 0) *(f32x2*)((float*)(ws + WS_LNST) + (size_t)row * 2) = (f32x2){mean, rstd};
.LBB0_1602:
	s_waitcnt vmcnt(4)
	v_mov_b32_e32 v40, v100
	v_mov_b32_e32 v41, v101
	v_mov_b32_e32 v44, v102
	v_mov_b32_e32 v45, v103
	v_mov_b32_e32 v52, v104
	v_mov_b32_e32 v53, v105
	v_mov_b32_e32 v56, v106
	v_mov_b32_e32 v57, v107
	s_add_u32 s8, s26, s28
	s_addc_u32 s9, s27, s29
	s_add_i32 vcc_lo, s5, s88
	s_cmp_lt_i32 vcc_lo, 0x10000
	s_cselect_b32 s8, s8, s26
	s_cselect_b32 s9, s9, s27
	v_lshl_add_u64 v[108:109], s[8:9], 0, v[36:37]
	global_load_dwordx2 v[100:101], v[108:109], off offset:1024
	global_load_dwordx2 v[102:103], v[108:109], off offset:1536
	global_load_dwordx2 v[104:105], v[108:109], off
	global_load_dwordx2 v[106:107], v[108:109], off offset:512
	v_lshlrev_b32_e32 v38, 16, v40
	v_and_b32_e32 v39, 0xffff0000, v40
	v_lshlrev_b32_e32 v49, 16, v53
	v_lshlrev_b32_e32 v48, 16, v52
	v_and_b32_e32 v55, 0xffff0000, v53
	v_and_b32_e32 v54, 0xffff0000, v52
	v_lshlrev_b32_e32 v53, 16, v57
	v_lshlrev_b32_e32 v52, 16, v56
	v_and_b32_e32 v57, 0xffff0000, v57
	v_and_b32_e32 v56, 0xffff0000, v56
	v_pk_add_f32 v[58:59], v[48:49], v[54:55]
	v_pk_add_f32 v[60:61], v[52:53], v[56:57]
	v_lshlrev_b32_e32 v42, 16, v41
	v_and_b32_e32 v43, 0xffff0000, v41
	v_and_b32_e32 v41, 0xffff0000, v44
	v_add_f32_e32 v40, v58, v59
	v_pk_add_f32 v[58:59], v[60:61], v[60:61] op_sel:[0,1] op_sel_hi:[1,0]
	v_lshlrev_b32_e32 v51, 16, v44
	v_lshlrev_b32_e32 v47, 16, v45
	v_and_b32_e32 v45, 0xffff0000, v45
	v_add_f32_e32 v46, v38, v39
	v_add_f32_e32 v44, v42, v43
	v_add_f32_e32 v50, 0, v40
	v_mov_b32_e32 v59, v41
	v_pk_add_f32 v[60:61], v[46:47], v[44:45]
	v_pk_add_f32 v[58:59], v[50:51], v[58:59]
	s_nop 0
	v_pk_add_f32 v[58:59], v[58:59], v[60:61]
	s_nop 0
	v_add_f32_e32 v40, v58, v59
	ds_bpermute_b32 v44, v1, v40
	s_waitcnt lgkmcnt(0)
	v_add_f32_e32 v40, v40, v44
	ds_bpermute_b32 v44, v62, v40
	s_waitcnt lgkmcnt(0)
	v_add_f32_e32 v40, v40, v44
	ds_bpermute_b32 v44, v63, v40
	s_waitcnt lgkmcnt(0)
	v_add_f32_e32 v40, v40, v44
	ds_bpermute_b32 v44, v64, v40
	s_waitcnt lgkmcnt(0)
	v_add_f32_e32 v40, v40, v44
	ds_bpermute_b32 v44, v65, v40
	s_waitcnt lgkmcnt(0)
	v_add_f32_e32 v40, v40, v44
	ds_bpermute_b32 v44, v66, v40
	s_waitcnt lgkmcnt(0)
	v_add_f32_e32 v40, v40, v44
	v_fmac_f32_e32 v55, 0xba800000, v40
	v_fmac_f32_e32 v49, 0xba800000, v40
	v_fmac_f32_e32 v54, 0xba800000, v40
	v_fmac_f32_e32 v57, 0xba800000, v40
	v_fmac_f32_e32 v53, 0xba800000, v40
	v_fmac_f32_e32 v56, 0xba800000, v40
	v_fmac_f32_e32 v48, 0xba800000, v40
	v_fmac_f32_e32 v52, 0xba800000, v40
	v_mov_b32_e32 v58, v49
	v_mov_b32_e32 v59, v55
	v_mov_b32_e32 v49, v54
	v_mov_b32_e32 v60, v53
	v_mov_b32_e32 v61, v57
	v_mov_b32_e32 v53, v56
	v_pk_mul_f32 v[70:71], v[58:59], v[58:59]
	v_pk_mul_f32 v[72:73], v[48:49], v[48:49]
	v_pk_mul_f32 v[74:75], v[60:61], v[60:61]
	v_pk_mul_f32 v[76:77], v[52:53], v[52:53]
	v_fmac_f32_e32 v42, 0xba800000, v40
	v_fmac_f32_e32 v38, 0xba800000, v40
	v_pk_mov_b32 v[82:83], v[72:73], v[70:71] op_sel:[1,0]
	v_mov_b32_e32 v73, v71
	v_pk_mov_b32 v[70:71], v[76:77], v[74:75] op_sel:[1,0]
	v_mov_b32_e32 v77, v75
	v_fmac_f32_e32 v43, 0xba800000, v40
	v_fmac_f32_e32 v39, 0xba800000, v40
	v_fmac_f32_e32 v45, 0xba800000, v40
	v_fmac_f32_e32 v47, 0xba800000, v40
	v_mul_f32_e32 v44, v38, v38
	v_mul_f32_e32 v46, v42, v42
	v_pk_add_f32 v[72:73], v[82:83], v[72:73]
	v_pk_add_f32 v[70:71], v[70:71], v[76:77]
	v_fmac_f32_e32 v41, 0xba800000, v40
	v_fmac_f32_e32 v51, 0xba800000, v40
	v_pk_fma_f32 v[78:79], v[38:39], v[38:39], v[44:45] op_sel_hi:[1,1,0]
	v_pk_fma_f32 v[80:81], v[42:43], v[42:43], v[46:47] op_sel_hi:[1,1,0]
	v_pk_add_f32 v[72:73], v[72:73], v[72:73] op_sel_hi:[0,1]
	v_pk_add_f32 v[70:71], v[70:71], v[70:71] op_sel_hi:[0,1]
	v_mul_f32_e32 v78, v51, v51
	v_mul_f32_e32 v80, v41, v41
	v_mul_f32_e32 v72, v47, v47
	v_mul_f32_e32 v70, v45, v45
	v_pk_add_f32 v[74:75], v[78:79], v[80:81]
	v_pk_add_f32 v[70:71], v[72:73], v[70:71]
	s_nop 0
	v_pk_add_f32 v[70:71], v[74:75], v[70:71]
	s_nop 0
	v_add_f32_e32 v44, v70, v71
	ds_bpermute_b32 v46, v1, v44
	s_waitcnt lgkmcnt(0)
	v_add_f32_e32 v44, v44, v46
	ds_bpermute_b32 v46, v62, v44
	s_waitcnt lgkmcnt(0)
	v_add_f32_e32 v44, v44, v46
	ds_bpermute_b32 v46, v63, v44
	s_waitcnt lgkmcnt(0)
	v_add_f32_e32 v44, v44, v46
	ds_bpermute_b32 v46, v64, v44
	s_waitcnt lgkmcnt(0)
	v_add_f32_e32 v44, v44, v46
	ds_bpermute_b32 v46, v65, v44
	s_waitcnt lgkmcnt(0)
	v_add_f32_e32 v44, v44, v46
	ds_bpermute_b32 v46, v66, v44
	s_waitcnt lgkmcnt(0)
	v_add_f32_e32 v44, v44, v46
	v_fmamk_f32 v44, v44, 0x3a800000, v67
	v_mul_f32_e32 v46, 0x4f800000, v44
	v_cmp_gt_f32_e32 vcc, s2, v44
	s_nop 1
	v_cndmask_b32_e32 v44, v44, v46, vcc
	v_sqrt_f32_e32 v46, v44
	s_nop 0
	v_add_u32_e32 v49, -1, v46
	v_add_u32_e32 v50, 1, v46
	v_fma_f32 v53, -v49, v46, v44
	v_fma_f32 v55, -v50, v46, v44
	v_cmp_ge_f32_e64 s[8:9], 0, v53
	s_nop 1
	v_cndmask_b32_e64 v46, v46, v49, s[8:9]
	v_cmp_lt_f32_e64 s[8:9], 0, v55
	s_nop 1
	v_cndmask_b32_e64 v46, v46, v50, s[8:9]
	v_mul_f32_e32 v49, 0x37800000, v46
	v_cndmask_b32_e32 v46, v46, v49, vcc
	v_cmp_class_f32_e32 vcc, v44, v68
	s_nop 1
	v_cndmask_b32_e32 v44, v46, v44, vcc
	v_div_scale_f32 v46, s[8:9], v44, v44, 1.0
	v_rcp_f32_e32 v49, v46
	v_div_scale_f32 v50, vcc, 1.0, v44, 1.0
	v_fma_f32 v53, -v46, v49, 1.0
	v_fmac_f32_e32 v49, v53, v49
	v_mul_f32_e32 v53, v50, v49
	v_fma_f32 v55, -v46, v53, v50
	v_fmac_f32_e32 v53, v55, v49
	v_fma_f32 v46, -v46, v53, v50
	v_div_fmas_f32 v46, v46, v49, v53
	v_div_fixup_f32 v46, v46, v44, 1.0
	s_and_saveexec_b64 s[8:9], s[6:7]
	s_cbranch_execz .LBB0_1601
	v_mul_f32_e32 v70, 0x3a800000, v40
	v_mov_b32_e32 v71, v46
	global_store_dwordx2 v35, v[70:71], s[18:19]
	s_branch .LBB0_1601
